# speedup vs baseline: 1.0014x; 1.0014x over previous
.LBB1_32:
	s_lshr_b32 s20, s3, 4
	s_bfe_u32 s21, s3, 0x20002
	s_and_b32 s22, s3, 3
	s_lshl_b32 s23, s20, 3
	s_lshl_b32 s24, s21, 1
	s_add_u32 s23, s23, s24
	s_lshl_b32 s25, s22, 14
	v_and_b32_e32 v130, 63, v0
	v_lshrrev_b32_e32 v131, 6, v0
	v_and_b32_e32 v132, 15, v130
	v_lshrrev_b32_e32 v133, 4, v130
	v_lshrrev_b32_e32 v134, 2, v131
	v_and_b32_e32 v135, 3, v131
	v_lshl_add_u32 v136, v135, 5, v132
	v_lshlrev_b32_e32 v136, 6, v136
	v_lshl_add_u32 v136, v133, 4, v136
	v_lshlrev_b32_e32 v137, 8, v134
	v_lshl_add_u32 v137, v133, 4, v137
	v_add_u32_e32 v137, 0x20000, v137
	v_readfirstlane_b32 s26, v134
	s_cmp_lg_u32 s26, 0
	s_cbranch_scc1 .Lqe_K
	v_mov_b32_e32 v138, 0x3fb8aa3b
	v_mov_b32_e32 v139, 0x3fb8aa3b
	s_add_u32 s27, s23, 0
	s_lshl_b32 s27, s27, 16
	s_add_u32 s27, s27, s25
	s_add_u32 s27, s27, 0x1500000
	v_add_u32_e32 v160, s27, v136
	v_add_u32_e32 v161, 0x2000, v160
	ds_read_b128 v[140:143], v137 offset:0
	ds_read_b128 v[144:147], v137 offset:64
	ds_read_b128 v[148:151], v137 offset:128
	ds_read_b128 v[152:155], v137 offset:192
	s_waitcnt lgkmcnt(0)
	v_pk_add_f32 v[126:127], v[126:127], v[140:141]
	v_pk_add_f32 v[128:129], v[128:129], v[142:143]
	v_pk_mul_f32 v[126:127], v[126:127], v[138:139]
	v_pk_mul_f32 v[128:129], v[128:129], v[138:139]
	v_cvt_pk_fp8_f32 v164, v126, v127
	v_cvt_pk_fp8_f32 v164, v128, v129 op_sel:[0,0,1]
	v_pk_add_f32 v[122:123], v[122:123], v[144:145]
	v_pk_add_f32 v[124:125], v[124:125], v[146:147]
	v_pk_mul_f32 v[122:123], v[122:123], v[138:139]
	v_pk_mul_f32 v[124:125], v[124:125], v[138:139]
	v_cvt_pk_fp8_f32 v165, v122, v123
	v_cvt_pk_fp8_f32 v165, v124, v125 op_sel:[0,0,1]
	v_pk_add_f32 v[118:119], v[118:119], v[148:149]
	v_pk_add_f32 v[120:121], v[120:121], v[150:151]
	v_pk_mul_f32 v[118:119], v[118:119], v[138:139]
	v_pk_mul_f32 v[120:121], v[120:121], v[138:139]
	v_cvt_pk_fp8_f32 v166, v118, v119
	v_cvt_pk_fp8_f32 v166, v120, v121 op_sel:[0,0,1]
	v_pk_add_f32 v[114:115], v[114:115], v[152:153]
	v_pk_add_f32 v[116:117], v[116:117], v[154:155]
	v_pk_mul_f32 v[114:115], v[114:115], v[138:139]
	v_pk_mul_f32 v[116:117], v[116:117], v[138:139]
	v_cvt_pk_fp8_f32 v167, v114, v115
	v_cvt_pk_fp8_f32 v167, v116, v117 op_sel:[0,0,1]
	s_nop 0
	global_store_dwordx4 v160, v[164:167], s[8:9]
	v_pk_add_f32 v[102:103], v[102:103], v[140:141]
	v_pk_add_f32 v[104:105], v[104:105], v[142:143]
	v_pk_mul_f32 v[102:103], v[102:103], v[138:139]
	v_pk_mul_f32 v[104:105], v[104:105], v[138:139]
	v_cvt_pk_fp8_f32 v168, v102, v103
	v_cvt_pk_fp8_f32 v168, v104, v105 op_sel:[0,0,1]
	v_pk_add_f32 v[98:99], v[98:99], v[144:145]
	v_pk_add_f32 v[100:101], v[100:101], v[146:147]
	v_pk_mul_f32 v[98:99], v[98:99], v[138:139]
	v_pk_mul_f32 v[100:101], v[100:101], v[138:139]
	v_cvt_pk_fp8_f32 v169, v98, v99
	v_cvt_pk_fp8_f32 v169, v100, v101 op_sel:[0,0,1]
	v_pk_add_f32 v[94:95], v[94:95], v[148:149]
	v_pk_add_f32 v[96:97], v[96:97], v[150:151]
	v_pk_mul_f32 v[94:95], v[94:95], v[138:139]
	v_pk_mul_f32 v[96:97], v[96:97], v[138:139]
	v_cvt_pk_fp8_f32 v170, v94, v95
	v_cvt_pk_fp8_f32 v170, v96, v97 op_sel:[0,0,1]
	v_pk_add_f32 v[90:91], v[90:91], v[152:153]
	v_pk_add_f32 v[92:93], v[92:93], v[154:155]
	v_pk_mul_f32 v[90:91], v[90:91], v[138:139]
	v_pk_mul_f32 v[92:93], v[92:93], v[138:139]
	v_cvt_pk_fp8_f32 v171, v90, v91
	v_cvt_pk_fp8_f32 v171, v92, v93 op_sel:[0,0,1]
	s_nop 0
	global_store_dwordx4 v160, v[168:171], s[8:9] offset:1024
	v_pk_add_f32 v[110:111], v[110:111], v[140:141]
	v_pk_add_f32 v[112:113], v[112:113], v[142:143]
	v_pk_mul_f32 v[110:111], v[110:111], v[138:139]
	v_pk_mul_f32 v[112:113], v[112:113], v[138:139]
	v_cvt_pk_fp8_f32 v164, v110, v111
	v_cvt_pk_fp8_f32 v164, v112, v113 op_sel:[0,0,1]
	v_pk_add_f32 v[106:107], v[106:107], v[144:145]
	v_pk_add_f32 v[108:109], v[108:109], v[146:147]
	v_pk_mul_f32 v[106:107], v[106:107], v[138:139]
	v_pk_mul_f32 v[108:109], v[108:109], v[138:139]
	v_cvt_pk_fp8_f32 v165, v106, v107
	v_cvt_pk_fp8_f32 v165, v108, v109 op_sel:[0,0,1]
	v_pk_add_f32 v[86:87], v[86:87], v[148:149]
	v_pk_add_f32 v[88:89], v[88:89], v[150:151]
	v_pk_mul_f32 v[86:87], v[86:87], v[138:139]
	v_pk_mul_f32 v[88:89], v[88:89], v[138:139]
	v_cvt_pk_fp8_f32 v166, v86, v87
	v_cvt_pk_fp8_f32 v166, v88, v89 op_sel:[0,0,1]
	v_pk_add_f32 v[82:83], v[82:83], v[152:153]
	v_pk_add_f32 v[84:85], v[84:85], v[154:155]
	v_pk_mul_f32 v[82:83], v[82:83], v[138:139]
	v_pk_mul_f32 v[84:85], v[84:85], v[138:139]
	v_cvt_pk_fp8_f32 v167, v82, v83
	v_cvt_pk_fp8_f32 v167, v84, v85 op_sel:[0,0,1]
	s_nop 0
	global_store_dwordx4 v161, v[164:167], s[8:9]
	v_pk_add_f32 v[78:79], v[78:79], v[140:141]
	v_pk_add_f32 v[80:81], v[80:81], v[142:143]
	v_pk_mul_f32 v[78:79], v[78:79], v[138:139]
	v_pk_mul_f32 v[80:81], v[80:81], v[138:139]
	v_cvt_pk_fp8_f32 v168, v78, v79
	v_cvt_pk_fp8_f32 v168, v80, v81 op_sel:[0,0,1]
	v_pk_add_f32 v[74:75], v[74:75], v[144:145]
	v_pk_add_f32 v[76:77], v[76:77], v[146:147]
	v_pk_mul_f32 v[74:75], v[74:75], v[138:139]
	v_pk_mul_f32 v[76:77], v[76:77], v[138:139]
	v_cvt_pk_fp8_f32 v169, v74, v75
	v_cvt_pk_fp8_f32 v169, v76, v77 op_sel:[0,0,1]
	v_pk_add_f32 v[70:71], v[70:71], v[148:149]
	v_pk_add_f32 v[72:73], v[72:73], v[150:151]
	v_pk_mul_f32 v[70:71], v[70:71], v[138:139]
	v_pk_mul_f32 v[72:73], v[72:73], v[138:139]
	v_cvt_pk_fp8_f32 v170, v70, v71
	v_cvt_pk_fp8_f32 v170, v72, v73 op_sel:[0,0,1]
	v_pk_add_f32 v[66:67], v[66:67], v[152:153]
	v_pk_add_f32 v[68:69], v[68:69], v[154:155]
	v_pk_mul_f32 v[66:67], v[66:67], v[138:139]
	v_pk_mul_f32 v[68:69], v[68:69], v[138:139]
	v_cvt_pk_fp8_f32 v171, v66, v67
	v_cvt_pk_fp8_f32 v171, v68, v69 op_sel:[0,0,1]
	s_nop 0
	global_store_dwordx4 v161, v[168:171], s[8:9] offset:1024
	s_add_u32 s27, s23, 1
	s_lshl_b32 s27, s27, 16
	s_add_u32 s27, s27, s25
	s_add_u32 s27, s27, 0x1500000
	v_add_u32_e32 v160, s27, v136
	v_add_u32_e32 v161, 0x2000, v160
	ds_read_b128 v[140:143], v137 offset:512
	ds_read_b128 v[144:147], v137 offset:576
	ds_read_b128 v[148:151], v137 offset:640
	ds_read_b128 v[152:155], v137 offset:704
	s_waitcnt lgkmcnt(0)
	v_pk_add_f32 v[62:63], v[62:63], v[140:141]
	v_pk_add_f32 v[64:65], v[64:65], v[142:143]
	v_pk_mul_f32 v[62:63], v[62:63], v[138:139]
	v_pk_mul_f32 v[64:65], v[64:65], v[138:139]
	v_cvt_pk_fp8_f32 v164, v62, v63
	v_cvt_pk_fp8_f32 v164, v64, v65 op_sel:[0,0,1]
	v_pk_add_f32 v[58:59], v[58:59], v[144:145]
	v_pk_add_f32 v[60:61], v[60:61], v[146:147]
	v_pk_mul_f32 v[58:59], v[58:59], v[138:139]
	v_pk_mul_f32 v[60:61], v[60:61], v[138:139]
	v_cvt_pk_fp8_f32 v165, v58, v59
	v_cvt_pk_fp8_f32 v165, v60, v61 op_sel:[0,0,1]
	v_pk_add_f32 v[54:55], v[54:55], v[148:149]
	v_pk_add_f32 v[56:57], v[56:57], v[150:151]
	v_pk_mul_f32 v[54:55], v[54:55], v[138:139]
	v_pk_mul_f32 v[56:57], v[56:57], v[138:139]
	v_cvt_pk_fp8_f32 v166, v54, v55
	v_cvt_pk_fp8_f32 v166, v56, v57 op_sel:[0,0,1]
	v_pk_add_f32 v[50:51], v[50:51], v[152:153]
	v_pk_add_f32 v[52:53], v[52:53], v[154:155]
	v_pk_mul_f32 v[50:51], v[50:51], v[138:139]
	v_pk_mul_f32 v[52:53], v[52:53], v[138:139]
	v_cvt_pk_fp8_f32 v167, v50, v51
	v_cvt_pk_fp8_f32 v167, v52, v53 op_sel:[0,0,1]
	s_nop 0
	global_store_dwordx4 v160, v[164:167], s[8:9]
	v_pk_add_f32 v[46:47], v[46:47], v[140:141]
	v_pk_add_f32 v[48:49], v[48:49], v[142:143]
	v_pk_mul_f32 v[46:47], v[46:47], v[138:139]
	v_pk_mul_f32 v[48:49], v[48:49], v[138:139]
	v_cvt_pk_fp8_f32 v168, v46, v47
	v_cvt_pk_fp8_f32 v168, v48, v49 op_sel:[0,0,1]
	v_pk_add_f32 v[42:43], v[42:43], v[144:145]
	v_pk_add_f32 v[44:45], v[44:45], v[146:147]
	v_pk_mul_f32 v[42:43], v[42:43], v[138:139]
	v_pk_mul_f32 v[44:45], v[44:45], v[138:139]
	v_cvt_pk_fp8_f32 v169, v42, v43
	v_cvt_pk_fp8_f32 v169, v44, v45 op_sel:[0,0,1]
	v_pk_add_f32 v[38:39], v[38:39], v[148:149]
	v_pk_add_f32 v[40:41], v[40:41], v[150:151]
	v_pk_mul_f32 v[38:39], v[38:39], v[138:139]
	v_pk_mul_f32 v[40:41], v[40:41], v[138:139]
	v_cvt_pk_fp8_f32 v170, v38, v39
	v_cvt_pk_fp8_f32 v170, v40, v41 op_sel:[0,0,1]
	v_pk_add_f32 v[34:35], v[34:35], v[152:153]
	v_pk_add_f32 v[36:37], v[36:37], v[154:155]
	v_pk_mul_f32 v[34:35], v[34:35], v[138:139]
	v_pk_mul_f32 v[36:37], v[36:37], v[138:139]
	v_cvt_pk_fp8_f32 v171, v34, v35
	v_cvt_pk_fp8_f32 v171, v36, v37 op_sel:[0,0,1]
	s_nop 0
	global_store_dwordx4 v160, v[168:171], s[8:9] offset:1024
	v_pk_add_f32 v[30:31], v[30:31], v[140:141]
	v_pk_add_f32 v[32:33], v[32:33], v[142:143]
	v_pk_mul_f32 v[30:31], v[30:31], v[138:139]
	v_pk_mul_f32 v[32:33], v[32:33], v[138:139]
	v_cvt_pk_fp8_f32 v164, v30, v31
	v_cvt_pk_fp8_f32 v164, v32, v33 op_sel:[0,0,1]
	v_pk_add_f32 v[26:27], v[26:27], v[144:145]
	v_pk_add_f32 v[28:29], v[28:29], v[146:147]
	v_pk_mul_f32 v[26:27], v[26:27], v[138:139]
	v_pk_mul_f32 v[28:29], v[28:29], v[138:139]
	v_cvt_pk_fp8_f32 v165, v26, v27
	v_cvt_pk_fp8_f32 v165, v28, v29 op_sel:[0,0,1]
	v_pk_add_f32 v[22:23], v[22:23], v[148:149]
	v_pk_add_f32 v[24:25], v[24:25], v[150:151]
	v_pk_mul_f32 v[22:23], v[22:23], v[138:139]
	v_pk_mul_f32 v[24:25], v[24:25], v[138:139]
	v_cvt_pk_fp8_f32 v166, v22, v23
	v_cvt_pk_fp8_f32 v166, v24, v25 op_sel:[0,0,1]
	v_pk_add_f32 v[14:15], v[14:15], v[152:153]
	v_pk_add_f32 v[16:17], v[16:17], v[154:155]
	v_pk_mul_f32 v[14:15], v[14:15], v[138:139]
	v_pk_mul_f32 v[16:17], v[16:17], v[138:139]
	v_cvt_pk_fp8_f32 v167, v14, v15
	v_cvt_pk_fp8_f32 v167, v16, v17 op_sel:[0,0,1]
	s_nop 0
	global_store_dwordx4 v161, v[164:167], s[8:9]
	v_pk_add_f32 v[10:11], v[10:11], v[140:141]
	v_pk_add_f32 v[12:13], v[12:13], v[142:143]
	v_pk_mul_f32 v[10:11], v[10:11], v[138:139]
	v_pk_mul_f32 v[12:13], v[12:13], v[138:139]
	v_cvt_pk_fp8_f32 v168, v10, v11
	v_cvt_pk_fp8_f32 v168, v12, v13 op_sel:[0,0,1]
	v_pk_add_f32 v[6:7], v[6:7], v[144:145]
	v_pk_add_f32 v[8:9], v[8:9], v[146:147]
	v_pk_mul_f32 v[6:7], v[6:7], v[138:139]
	v_pk_mul_f32 v[8:9], v[8:9], v[138:139]
	v_cvt_pk_fp8_f32 v169, v6, v7
	v_cvt_pk_fp8_f32 v169, v8, v9 op_sel:[0,0,1]
	v_pk_add_f32 v[2:3], v[2:3], v[148:149]
	v_pk_add_f32 v[4:5], v[4:5], v[150:151]
	v_pk_mul_f32 v[2:3], v[2:3], v[138:139]
	v_pk_mul_f32 v[4:5], v[4:5], v[138:139]
	v_cvt_pk_fp8_f32 v170, v2, v3
	v_cvt_pk_fp8_f32 v170, v4, v5 op_sel:[0,0,1]
	v_pk_add_f32 v[18:19], v[18:19], v[152:153]
	v_pk_add_f32 v[20:21], v[20:21], v[154:155]
	v_pk_mul_f32 v[18:19], v[18:19], v[138:139]
	v_pk_mul_f32 v[20:21], v[20:21], v[138:139]
	v_cvt_pk_fp8_f32 v171, v18, v19
	v_cvt_pk_fp8_f32 v171, v20, v21 op_sel:[0,0,1]
	s_nop 0
	global_store_dwordx4 v161, v[168:171], s[8:9] offset:1024
	s_endpgm
.Lqe_K:
	s_add_u32 s27, s23, 0
	s_mul_i32 s27, s27, 0x12000
	s_add_u32 s27, s27, s25
	s_add_u32 s27, s27, 0x2502000
	v_add_u32_e32 v160, s27, v136
	v_add_u32_e32 v161, 0x2000, v160
	ds_read_b128 v[140:143], v137 offset:0
	ds_read_b128 v[144:147], v137 offset:64
	ds_read_b128 v[148:151], v137 offset:128
	ds_read_b128 v[152:155], v137 offset:192
	s_waitcnt lgkmcnt(0)
	v_pk_add_f32 v[126:127], v[126:127], v[140:141]
	v_pk_add_f32 v[128:129], v[128:129], v[142:143]
	v_cvt_pk_fp8_f32 v164, v126, v127
	v_cvt_pk_fp8_f32 v164, v128, v129 op_sel:[0,0,1]
	v_pk_add_f32 v[122:123], v[122:123], v[144:145]
	v_pk_add_f32 v[124:125], v[124:125], v[146:147]
	v_cvt_pk_fp8_f32 v165, v122, v123
	v_cvt_pk_fp8_f32 v165, v124, v125 op_sel:[0,0,1]
	v_pk_add_f32 v[118:119], v[118:119], v[148:149]
	v_pk_add_f32 v[120:121], v[120:121], v[150:151]
	v_cvt_pk_fp8_f32 v166, v118, v119
	v_cvt_pk_fp8_f32 v166, v120, v121 op_sel:[0,0,1]
	v_pk_add_f32 v[114:115], v[114:115], v[152:153]
	v_pk_add_f32 v[116:117], v[116:117], v[154:155]
	v_cvt_pk_fp8_f32 v167, v114, v115
	v_cvt_pk_fp8_f32 v167, v116, v117 op_sel:[0,0,1]
	s_nop 0
	global_store_dwordx4 v160, v[164:167], s[8:9]
	v_pk_add_f32 v[102:103], v[102:103], v[140:141]
	v_pk_add_f32 v[104:105], v[104:105], v[142:143]
	v_cvt_pk_fp8_f32 v168, v102, v103
	v_cvt_pk_fp8_f32 v168, v104, v105 op_sel:[0,0,1]
	v_pk_add_f32 v[98:99], v[98:99], v[144:145]
	v_pk_add_f32 v[100:101], v[100:101], v[146:147]
	v_cvt_pk_fp8_f32 v169, v98, v99
	v_cvt_pk_fp8_f32 v169, v100, v101 op_sel:[0,0,1]
	v_pk_add_f32 v[94:95], v[94:95], v[148:149]
	v_pk_add_f32 v[96:97], v[96:97], v[150:151]
	v_cvt_pk_fp8_f32 v170, v94, v95
	v_cvt_pk_fp8_f32 v170, v96, v97 op_sel:[0,0,1]
	v_pk_add_f32 v[90:91], v[90:91], v[152:153]
	v_pk_add_f32 v[92:93], v[92:93], v[154:155]
	v_cvt_pk_fp8_f32 v171, v90, v91
	v_cvt_pk_fp8_f32 v171, v92, v93 op_sel:[0,0,1]
	s_nop 0
	global_store_dwordx4 v160, v[168:171], s[8:9] offset:1024
	v_pk_add_f32 v[110:111], v[110:111], v[140:141]
	v_pk_add_f32 v[112:113], v[112:113], v[142:143]
	v_cvt_pk_fp8_f32 v164, v110, v111
	v_cvt_pk_fp8_f32 v164, v112, v113 op_sel:[0,0,1]
	v_pk_add_f32 v[106:107], v[106:107], v[144:145]
	v_pk_add_f32 v[108:109], v[108:109], v[146:147]
	v_cvt_pk_fp8_f32 v165, v106, v107
	v_cvt_pk_fp8_f32 v165, v108, v109 op_sel:[0,0,1]
	v_pk_add_f32 v[86:87], v[86:87], v[148:149]
	v_pk_add_f32 v[88:89], v[88:89], v[150:151]
	v_cvt_pk_fp8_f32 v166, v86, v87
	v_cvt_pk_fp8_f32 v166, v88, v89 op_sel:[0,0,1]
	v_pk_add_f32 v[82:83], v[82:83], v[152:153]
	v_pk_add_f32 v[84:85], v[84:85], v[154:155]
	v_cvt_pk_fp8_f32 v167, v82, v83
	v_cvt_pk_fp8_f32 v167, v84, v85 op_sel:[0,0,1]
	s_nop 0
	global_store_dwordx4 v161, v[164:167], s[8:9]
	v_pk_add_f32 v[78:79], v[78:79], v[140:141]
	v_pk_add_f32 v[80:81], v[80:81], v[142:143]
	v_cvt_pk_fp8_f32 v168, v78, v79
	v_cvt_pk_fp8_f32 v168, v80, v81 op_sel:[0,0,1]
	v_pk_add_f32 v[74:75], v[74:75], v[144:145]
	v_pk_add_f32 v[76:77], v[76:77], v[146:147]
	v_cvt_pk_fp8_f32 v169, v74, v75
	v_cvt_pk_fp8_f32 v169, v76, v77 op_sel:[0,0,1]
	v_pk_add_f32 v[70:71], v[70:71], v[148:149]
	v_pk_add_f32 v[72:73], v[72:73], v[150:151]
	v_cvt_pk_fp8_f32 v170, v70, v71
	v_cvt_pk_fp8_f32 v170, v72, v73 op_sel:[0,0,1]
	v_pk_add_f32 v[66:67], v[66:67], v[152:153]
	v_pk_add_f32 v[68:69], v[68:69], v[154:155]
	v_cvt_pk_fp8_f32 v171, v66, v67
	v_cvt_pk_fp8_f32 v171, v68, v69 op_sel:[0,0,1]
	s_nop 0
	global_store_dwordx4 v161, v[168:171], s[8:9] offset:1024
	s_add_u32 s27, s23, 1
	s_mul_i32 s27, s27, 0x12000
	s_add_u32 s27, s27, s25
	s_add_u32 s27, s27, 0x2502000
	v_add_u32_e32 v160, s27, v136
	v_add_u32_e32 v161, 0x2000, v160
	ds_read_b128 v[140:143], v137 offset:512
	ds_read_b128 v[144:147], v137 offset:576
	ds_read_b128 v[148:151], v137 offset:640
	ds_read_b128 v[152:155], v137 offset:704
	s_waitcnt lgkmcnt(0)
	v_pk_add_f32 v[62:63], v[62:63], v[140:141]
	v_pk_add_f32 v[64:65], v[64:65], v[142:143]
	v_cvt_pk_fp8_f32 v164, v62, v63
	v_cvt_pk_fp8_f32 v164, v64, v65 op_sel:[0,0,1]
	v_pk_add_f32 v[58:59], v[58:59], v[144:145]
	v_pk_add_f32 v[60:61], v[60:61], v[146:147]
	v_cvt_pk_fp8_f32 v165, v58, v59
	v_cvt_pk_fp8_f32 v165, v60, v61 op_sel:[0,0,1]
	v_pk_add_f32 v[54:55], v[54:55], v[148:149]
	v_pk_add_f32 v[56:57], v[56:57], v[150:151]
	v_cvt_pk_fp8_f32 v166, v54, v55
	v_cvt_pk_fp8_f32 v166, v56, v57 op_sel:[0,0,1]
	v_pk_add_f32 v[50:51], v[50:51], v[152:153]
	v_pk_add_f32 v[52:53], v[52:53], v[154:155]
	v_cvt_pk_fp8_f32 v167, v50, v51
	v_cvt_pk_fp8_f32 v167, v52, v53 op_sel:[0,0,1]
	s_nop 0
	global_store_dwordx4 v160, v[164:167], s[8:9]
	v_pk_add_f32 v[46:47], v[46:47], v[140:141]
	v_pk_add_f32 v[48:49], v[48:49], v[142:143]
	v_cvt_pk_fp8_f32 v168, v46, v47
	v_cvt_pk_fp8_f32 v168, v48, v49 op_sel:[0,0,1]
	v_pk_add_f32 v[42:43], v[42:43], v[144:145]
	v_pk_add_f32 v[44:45], v[44:45], v[146:147]
	v_cvt_pk_fp8_f32 v169, v42, v43
	v_cvt_pk_fp8_f32 v169, v44, v45 op_sel:[0,0,1]
	v_pk_add_f32 v[38:39], v[38:39], v[148:149]
	v_pk_add_f32 v[40:41], v[40:41], v[150:151]
	v_cvt_pk_fp8_f32 v170, v38, v39
	v_cvt_pk_fp8_f32 v170, v40, v41 op_sel:[0,0,1]
	v_pk_add_f32 v[34:35], v[34:35], v[152:153]
	v_pk_add_f32 v[36:37], v[36:37], v[154:155]
	v_cvt_pk_fp8_f32 v171, v34, v35
	v_cvt_pk_fp8_f32 v171, v36, v37 op_sel:[0,0,1]
	s_nop 0
	global_store_dwordx4 v160, v[168:171], s[8:9] offset:1024
	v_pk_add_f32 v[30:31], v[30:31], v[140:141]
	v_pk_add_f32 v[32:33], v[32:33], v[142:143]
	v_cvt_pk_fp8_f32 v164, v30, v31
	v_cvt_pk_fp8_f32 v164, v32, v33 op_sel:[0,0,1]
	v_pk_add_f32 v[26:27], v[26:27], v[144:145]
	v_pk_add_f32 v[28:29], v[28:29], v[146:147]
	v_cvt_pk_fp8_f32 v165, v26, v27
	v_cvt_pk_fp8_f32 v165, v28, v29 op_sel:[0,0,1]
	v_pk_add_f32 v[22:23], v[22:23], v[148:149]
	v_pk_add_f32 v[24:25], v[24:25], v[150:151]
	v_cvt_pk_fp8_f32 v166, v22, v23
	v_cvt_pk_fp8_f32 v166, v24, v25 op_sel:[0,0,1]
	v_pk_add_f32 v[14:15], v[14:15], v[152:153]
	v_pk_add_f32 v[16:17], v[16:17], v[154:155]
	v_cvt_pk_fp8_f32 v167, v14, v15
	v_cvt_pk_fp8_f32 v167, v16, v17 op_sel:[0,0,1]
	s_nop 0
	global_store_dwordx4 v161, v[164:167], s[8:9]
	v_pk_add_f32 v[10:11], v[10:11], v[140:141]
	v_pk_add_f32 v[12:13], v[12:13], v[142:143]
	v_cvt_pk_fp8_f32 v168, v10, v11
	v_cvt_pk_fp8_f32 v168, v12, v13 op_sel:[0,0,1]
	v_pk_add_f32 v[6:7], v[6:7], v[144:145]
	v_pk_add_f32 v[8:9], v[8:9], v[146:147]
	v_cvt_pk_fp8_f32 v169, v6, v7
	v_cvt_pk_fp8_f32 v169, v8, v9 op_sel:[0,0,1]
	v_pk_add_f32 v[2:3], v[2:3], v[148:149]
	v_pk_add_f32 v[4:5], v[4:5], v[150:151]
	v_cvt_pk_fp8_f32 v170, v2, v3
	v_cvt_pk_fp8_f32 v170, v4, v5 op_sel:[0,0,1]
	v_pk_add_f32 v[18:19], v[18:19], v[152:153]
	v_pk_add_f32 v[20:21], v[20:21], v[154:155]
	v_cvt_pk_fp8_f32 v171, v18, v19
	v_cvt_pk_fp8_f32 v171, v20, v21 op_sel:[0,0,1]
	s_nop 0
	global_store_dwordx4 v161, v[168:171], s[8:9] offset:1024
	s_endpgm
